# v16: v13 + ph4 next-unit L2 prefetch + xor-1/2/8 lane exchanges via DPP instead of ds_bpermute in the attention part-store epilogue and the ph4 rmsnorm reduction
# speedup vs baseline: 1.0019x; 1.0019x over previous
; __device__ __forceinline__ void ph4_unit(const Frame& F, const Args& A, int c, int h) {
;     ...
;         bf16* QF = (bf16*)(ws + WS_QF); bf16* KF = (bf16*)(ws + WS_KF);
;         const float gq0 = A.in[I_FQG][h * 128 + 2 * lane], gq1 = A.in[I_FQG][h * 128 + 2 * lane + 1], gk0 = A.in[I_FKG][h * 128 + 2 * lane], gk1 = A.in[I_FKG][h * 128 + 2 * lane + 1];
;         float rl;
;         { float s0[16], s1[8], s2[4], s3[2];
;           const bool b0 = lane & 1, b1 = lane & 2, b2 = lane & 4, b3 = lane & 8;
; #pragma unroll
;           for (int i = 0; i < 16; ++i) { const float x0 = bflo(qw[i]), x1 = bfhi(qw[i]); s0[i] = x0 * x0 + x1 * x1; }
; #pragma unroll
;           for (int k = 0; k < 8; ++k) s1[k] = (b0 ? s0[2 * k + 1] : s0[2 * k]) + __shfl_xor(b0 ? s0[2 * k] : s0[2 * k + 1], 1);
; #pragma unroll
;           for (int k = 0; k < 4; ++k) s2[k] = (b1 ? s1[2 * k + 1] : s1[2 * k]) + __shfl_xor(b1 ? s1[2 * k] : s1[2 * k + 1], 2);
; #pragma unroll
;           for (int k = 0; k < 2; ++k) s3[k] = (b2 ? s2[2 * k + 1] : s2[2 * k]) + __shfl_xor(b2 ? s2[2 * k] : s2[2 * k + 1], 4);
;           float s4 = (b3 ? s3[1] : s3[0]) + __shfl_xor(b3 ? s3[0] : s3[1], 8);
;           s4 += __shfl_xor(s4, 16); s4 += __shfl_xor(s4, 32);
;           rl = __builtin_amdgcn_rsqf(s4 * (1.f / 128.f) + EPS_); }
.LBB0_333:
	s_or_b64 exec, exec, s[50:51]
	v_lshlrev_b32_e32 v82, 16, v63
	v_and_b32_e32 v83, 0xffff0000, v63
	v_and_b32_e32 v63, 64, v97
	v_lshlrev_b32_e32 v72, 16, v66
	v_and_b32_e32 v73, 0xffff0000, v66
	v_lshlrev_b32_e32 v70, 16, v67
	v_and_b32_e32 v71, 0xffff0000, v67
	v_lshlrev_b32_e32 v66, 16, v74
	v_and_b32_e32 v67, 0xffff0000, v74
	v_xor_b32_e32 v18, 1, v97
	v_add_u32_e32 v74, 64, v63
	v_cmp_lt_i32_e32 vcc, v18, v74
	v_lshlrev_b32_e32 v6, 16, v105
	v_and_b32_e32 v7, 0xffff0000, v105
	v_cndmask_b32_e32 v18, v97, v18, vcc
	v_lshlrev_b32_e32 v105, 2, v18
	v_xor_b32_e32 v18, 2, v97
	v_cmp_lt_i32_e32 vcc, v18, v74
	v_lshlrev_b32_e32 v8, 16, v104
	v_and_b32_e32 v9, 0xffff0000, v104
	v_cndmask_b32_e32 v18, v97, v18, vcc
	v_lshlrev_b32_e32 v104, 2, v18
	v_xor_b32_e32 v18, 4, v97
	v_or_b32_e32 v2, s33, v20
	v_lshlrev_b32_e32 v78, 16, v64
	v_and_b32_e32 v79, 0xffff0000, v64
	v_cmp_lt_i32_e32 vcc, v18, v74
	v_lshlrev_b32_e32 v108, 2, v2
	v_lshlrev_b32_e32 v16, 16, v80
	v_and_b32_e32 v17, 0xffff0000, v80
	v_lshlrev_b32_e32 v14, 16, v81
	v_and_b32_e32 v15, 0xffff0000, v81
	v_lshlrev_b32_e32 v4, 16, v106
	v_and_b32_e32 v5, 0xffff0000, v106
	v_lshlrev_b32_e32 v2, 16, v107
	v_and_b32_e32 v3, 0xffff0000, v107
	v_cndmask_b32_e32 v18, v97, v18, vcc
	v_pk_mul_f32 v[80:81], v[82:83], v[82:83]
	v_pk_mul_f32 v[106:107], v[78:79], v[78:79]
	v_lshlrev_b32_e32 v10, 16, v103
	v_and_b32_e32 v11, 0xffff0000, v103
	v_lshlrev_b32_e32 v103, 2, v18
	v_xor_b32_e32 v18, 8, v97
	v_add_f32_e32 v109, v80, v81
	v_add_f32_e32 v106, v106, v107
	v_cmp_lt_i32_e32 vcc, v18, v74
	v_cndmask_b32_e64 v107, v106, v109, s[20:21]
	v_cndmask_b32_e64 v106, v109, v106, s[20:21]
	v_cndmask_b32_e32 v18, v97, v18, vcc
	s_nop 1
	v_mov_b32_dpp v106, v106 quad_perm:[1,0,3,2] row_mask:0xf bank_mask:0xf
	v_lshlrev_b32_e32 v12, 16, v102
	v_and_b32_e32 v13, 0xffff0000, v102
	v_lshlrev_b32_e32 v102, 2, v18
	v_xor_b32_e32 v18, 16, v97
	v_cmp_lt_i32_e32 vcc, v18, v74
	v_readlane_b32 s0, v254, 16
	v_lshlrev_b32_e32 v76, 16, v65
	v_cndmask_b32_e32 v18, v97, v18, vcc
	v_and_b32_e32 v77, 0xffff0000, v65
	v_lshlrev_b32_e32 v63, 2, v18
	v_xor_b32_e32 v18, 32, v97
	v_readlane_b32 s8, v254, 24
	v_readlane_b32 s9, v254, 25
	v_readlane_b32 s10, v254, 26
	v_readlane_b32 s11, v254, 27
	v_lshlrev_b32_e32 v64, 16, v75
	v_and_b32_e32 v65, 0xffff0000, v75
	v_cmp_lt_i32_e32 vcc, v18, v74
	global_load_dwordx2 v[74:75], v108, s[8:9]
	v_lshlrev_b32_e32 v68, 16, v69
	global_load_dwordx2 v[80:81], v108, s[10:11]
	v_readlane_b32 s98, v254, 49
	s_add_i32 s98, s58, s98
	s_and_b32 s99, s98, 7
	s_ashr_i32 s98, s98, 3
	s_lshl_b32 s98, s98, 6
	v_lshrrev_b32_e32 v124, 3, v0
	v_add_u32_e32 v124, s98, v124
	v_mul_u32_u24_e32 v124, 0x5800, v124
	v_and_b32_e32 v126, 1, v0
	v_bfe_u32 v125, v0, 1, 2
	v_min_u32_e32 v127, 1, v125
	v_lshrrev_b32_e32 v128, 1, v125
	v_add_u32_e32 v128, v128, v125
	v_lshlrev_b32_e32 v128, 11, v128
	v_mul_u32_u24_e32 v129, 0x380, v127
	v_sub_u32_e32 v129, 0x400, v129
	v_mad_u32_u24 v128, v126, v129, v128
	v_lshlrev_b32_e32 v129, 7, v127
	v_add_u32_e32 v129, 0x80, v129
	v_mul_u32_u24_e32 v129, s99, v129
	v_add3_u32 v124, v124, v128, v129
	global_load_dword v130, v124, s[28:29]
	s_waitcnt lgkmcnt(0)
	v_add_f32_e32 v108, v107, v106
	v_pk_mul_f32 v[106:107], v[76:77], v[76:77]
	v_and_b32_e32 v69, 0xffff0000, v69
	v_add_f32_e32 v109, v106, v107
	v_pk_mul_f32 v[106:107], v[72:73], v[72:73]
	v_readlane_b32 s1, v254, 17
	v_add_f32_e32 v106, v106, v107
	v_cndmask_b32_e64 v107, v106, v109, s[20:21]
	v_cndmask_b32_e64 v106, v109, v106, s[20:21]
	s_nop 1
	v_mov_b32_dpp v106, v106 quad_perm:[1,0,3,2] row_mask:0xf bank_mask:0xf
	s_lshl_b64 s[0:1], s[96:97], 11
	s_add_u32 s50, s37, s0
	s_addc_u32 s51, s52, s1
	s_lshl_b32 s30, s33, 1
	s_waitcnt lgkmcnt(0)
	v_add_f32_e32 v106, v107, v106
	v_cndmask_b32_e64 v107, v106, v108, s[24:25]
	v_cndmask_b32_e64 v106, v108, v106, s[24:25]
	s_nop 1
	v_mov_b32_dpp v106, v106 quad_perm:[2,3,0,1] row_mask:0xf bank_mask:0xf
	s_add_u32 s50, s50, s30
	s_addc_u32 s51, s51, 0
	s_add_u32 s0, s53, s0
	s_addc_u32 s1, s54, s1
	s_waitcnt lgkmcnt(0)
	v_add_f32_e32 v108, v107, v106
	v_pk_mul_f32 v[106:107], v[70:71], v[70:71]
	s_add_u32 s84, s0, s30
	v_add_f32_e32 v109, v106, v107
	v_pk_mul_f32 v[106:107], v[68:69], v[68:69]
	s_addc_u32 s85, s1, 0
	v_add_f32_e32 v106, v106, v107
	v_cndmask_b32_e64 v107, v106, v109, s[20:21]
	v_cndmask_b32_e64 v106, v109, v106, s[20:21]
	s_nop 1
	v_mov_b32_dpp v106, v106 quad_perm:[1,0,3,2] row_mask:0xf bank_mask:0xf
	s_lshl_b64 s[0:1], s[80:81], 11
	s_add_u32 s33, s37, s0
	s_addc_u32 s59, s52, s1
	s_add_u32 s80, s33, s30
	s_waitcnt lgkmcnt(0)
	v_add_f32_e32 v109, v107, v106
	v_pk_mul_f32 v[106:107], v[66:67], v[66:67]
	s_addc_u32 s81, s59, 0
	v_add_f32_e32 v110, v106, v107
	v_pk_mul_f32 v[106:107], v[64:65], v[64:65]
	s_add_u32 s0, s53, s0
	v_add_f32_e32 v106, v106, v107
	v_cndmask_b32_e64 v107, v106, v110, s[20:21]
	v_cndmask_b32_e64 v106, v110, v106, s[20:21]
	s_nop 1
	v_mov_b32_dpp v106, v106 quad_perm:[1,0,3,2] row_mask:0xf bank_mask:0xf
	s_addc_u32 s1, s54, s1
	s_add_u32 s86, s0, s30
	s_addc_u32 s87, s1, 0
	s_lshl_b64 s[0:1], s[76:77], 11
	s_waitcnt lgkmcnt(0)
	v_add_f32_e32 v106, v107, v106
	v_cndmask_b32_e64 v107, v106, v109, s[24:25]
	v_cndmask_b32_e64 v106, v109, v106, s[24:25]
	s_nop 1
	v_mov_b32_dpp v106, v106 quad_perm:[2,3,0,1] row_mask:0xf bank_mask:0xf
	s_add_u32 s33, s37, s0
	s_addc_u32 s59, s52, s1
	s_add_u32 s76, s33, s30
	s_addc_u32 s77, s59, 0
	s_waitcnt lgkmcnt(0)
	v_add_f32_e32 v106, v107, v106
	v_cndmask_b32_e64 v107, v106, v108, s[22:23]
	v_cndmask_b32_e64 v106, v108, v106, s[22:23]
	ds_bpermute_b32 v106, v103, v106
	s_add_u32 s0, s53, s0
	s_addc_u32 s1, s54, s1
	s_add_u32 s92, s0, s30
	s_addc_u32 s93, s1, 0
	s_waitcnt lgkmcnt(0)
; __device__ __forceinline__ void ph4_unit(const Frame& F, const Args& A, int c, int h) {
;     ...
;           for (int k = 0; k < 8; ++k) s1[k] = (b0 ? s0[2 * k + 1] : s0[2 * k]) + __shfl_xor(b0 ? s0[2 * k] : s0[2 * k + 1], 1);
; #pragma unroll
;           for (int k = 0; k < 4; ++k) s2[k] = (b1 ? s1[2 * k + 1] : s1[2 * k]) + __shfl_xor(b1 ? s1[2 * k] : s1[2 * k + 1], 2);
; #pragma unroll
;           for (int k = 0; k < 2; ++k) s3[k] = (b2 ? s2[2 * k + 1] : s2[2 * k]) + __shfl_xor(b2 ? s2[2 * k] : s2[2 * k + 1], 4);
;           float s4 = (b3 ? s3[1] : s3[0]) + __shfl_xor(b3 ? s3[0] : s3[1], 8);
;           s4 += __shfl_xor(s4, 16); s4 += __shfl_xor(s4, 32);
;           rl = __builtin_amdgcn_rsqf(s4 * (1.f / 128.f) + EPS_); }
	v_add_f32_e32 v108, v107, v106
	v_pk_mul_f32 v[106:107], v[16:17], v[16:17]
	s_lshl_b64 s[0:1], s[72:73], 11
	v_add_f32_e32 v109, v106, v107
	v_pk_mul_f32 v[106:107], v[14:15], v[14:15]
	s_add_u32 s33, s37, s0
	v_add_f32_e32 v106, v106, v107
	v_cndmask_b32_e64 v107, v106, v109, s[20:21]
	v_cndmask_b32_e64 v106, v109, v106, s[20:21]
	s_nop 1
	v_mov_b32_dpp v106, v106 quad_perm:[1,0,3,2] row_mask:0xf bank_mask:0xf
	s_addc_u32 s59, s52, s1
	v_cndmask_b32_e32 v18, v97, v18, vcc
	s_add_u32 s72, s33, s30
	v_lshlrev_b32_e32 v18, 2, v18
	s_waitcnt lgkmcnt(0)
	v_add_f32_e32 v109, v107, v106
	v_pk_mul_f32 v[106:107], v[12:13], v[12:13]
	s_addc_u32 s73, s59, 0
	v_add_f32_e32 v110, v106, v107
	v_pk_mul_f32 v[106:107], v[10:11], v[10:11]
	s_add_u32 s0, s53, s0
	v_add_f32_e32 v106, v106, v107
	v_cndmask_b32_e64 v107, v106, v110, s[20:21]
	v_cndmask_b32_e64 v106, v110, v106, s[20:21]
	s_nop 1
	v_mov_b32_dpp v106, v106 quad_perm:[1,0,3,2] row_mask:0xf bank_mask:0xf
	s_addc_u32 s1, s54, s1
	s_add_u32 s94, s0, s30
	s_addc_u32 s95, s1, 0
	s_lshl_b64 s[0:1], s[68:69], 11
	s_waitcnt lgkmcnt(0)
	v_add_f32_e32 v106, v107, v106
	v_cndmask_b32_e64 v107, v106, v109, s[24:25]
	v_cndmask_b32_e64 v106, v109, v106, s[24:25]
	s_nop 1
	v_mov_b32_dpp v106, v106 quad_perm:[2,3,0,1] row_mask:0xf bank_mask:0xf
	s_add_u32 s33, s37, s0
	s_addc_u32 s59, s52, s1
	s_add_u32 s68, s33, s30
	s_addc_u32 s69, s59, 0
	s_waitcnt lgkmcnt(0)
	v_add_f32_e32 v109, v107, v106
	v_pk_mul_f32 v[106:107], v[8:9], v[8:9]
	s_add_u32 s0, s53, s0
	v_add_f32_e32 v110, v106, v107
	v_pk_mul_f32 v[106:107], v[6:7], v[6:7]
	s_addc_u32 s1, s54, s1
	v_add_f32_e32 v106, v106, v107
	v_cndmask_b32_e64 v107, v106, v110, s[20:21]
	v_cndmask_b32_e64 v106, v110, v106, s[20:21]
	s_nop 1
	v_mov_b32_dpp v106, v106 quad_perm:[1,0,3,2] row_mask:0xf bank_mask:0xf
	s_add_u32 s96, s0, s30
	s_addc_u32 s97, s1, 0
	s_lshl_b64 s[0:1], s[66:67], 11
	s_add_u32 s33, s37, s0
	s_waitcnt lgkmcnt(0)
	v_add_f32_e32 v110, v107, v106
	v_pk_mul_f32 v[106:107], v[4:5], v[4:5]
	s_addc_u32 s59, s52, s1
	v_add_f32_e32 v111, v106, v107
	v_pk_mul_f32 v[106:107], v[2:3], v[2:3]
	s_add_u32 s66, s33, s30
	v_add_f32_e32 v106, v106, v107
	v_cndmask_b32_e64 v107, v106, v111, s[20:21]
	v_cndmask_b32_e64 v106, v111, v106, s[20:21]
	s_nop 1
	v_mov_b32_dpp v105, v106 quad_perm:[1,0,3,2] row_mask:0xf bank_mask:0xf
	s_addc_u32 s67, s59, 0
	s_add_u32 s0, s53, s0
	s_addc_u32 s1, s54, s1
	s_add_u32 vcc_lo, s0, s30
	s_waitcnt lgkmcnt(0)
	v_add_f32_e32 v105, v107, v105
	v_cndmask_b32_e64 v106, v105, v110, s[24:25]
	v_cndmask_b32_e64 v105, v110, v105, s[24:25]
	s_nop 1
	v_mov_b32_dpp v104, v105 quad_perm:[2,3,0,1] row_mask:0xf bank_mask:0xf
	s_addc_u32 vcc_hi, s1, 0
	s_lshl_b64 s[0:1], s[64:65], 11
	s_add_u32 s33, s37, s0
	s_addc_u32 s59, s52, s1
	s_waitcnt lgkmcnt(0)
	v_add_f32_e32 v104, v106, v104
	v_cndmask_b32_e64 v105, v104, v109, s[22:23]
	v_cndmask_b32_e64 v104, v109, v104, s[22:23]
	ds_bpermute_b32 v103, v103, v104
	s_add_u32 s64, s33, s30
	s_addc_u32 s65, s59, 0
	s_add_u32 s0, s53, s0
	s_addc_u32 s1, s54, s1
	s_waitcnt lgkmcnt(0)
	v_add_f32_e32 v103, v105, v103
	v_cndmask_b32_e64 v104, v103, v108, s[26:27]
	v_cndmask_b32_e64 v103, v108, v103, s[26:27]
	s_nop 1
	v_mov_b32_dpp v102, v103 row_ror:8 row_mask:0xf bank_mask:0xf
	s_add_u32 s90, s0, s30
	s_addc_u32 s91, s1, 0
	s_lshl_b64 s[48:49], s[48:49], 11
	s_add_u32 s0, s37, s48
	s_waitcnt lgkmcnt(0)
	v_add_f32_e32 v102, v104, v102
	ds_bpermute_b32 v63, v63, v102
	s_addc_u32 s1, s52, s49
	s_add_u32 s0, s0, s30
	s_addc_u32 s1, s1, 0
	v_readlane_b32 s2, v254, 18
	s_waitcnt lgkmcnt(0)
	v_add_f32_e32 v63, v102, v63
	ds_bpermute_b32 v18, v18, v63
	v_readlane_b32 s3, v254, 19
	v_readlane_b32 s4, v254, 20
	v_readlane_b32 s5, v254, 21
	v_readlane_b32 s6, v254, 22
	s_waitcnt lgkmcnt(0)
; __device__ __forceinline__ unsigned pk2(float lo, float hi) { const f32x2_t v = {lo, hi}; return __builtin_bit_cast(unsigned, __builtin_convertvector(v, bf16x2_hw)); }
; __device__ __forceinline__ void ph4_unit(const Frame& F, const Args& A, int c, int h) {
;     ...
;           rl = __builtin_amdgcn_rsqf(s4 * (1.f / 128.f) + EPS_); }
; #pragma unroll
;         for (int i = 0; i < 16; ++i) { const int rv = F.wave * 16 + i, t = rv >> 1, isk2 = rv & 1; const float x0 = bflo(qw[i]), x1 = bfhi(qw[i]);
;             const float r = __builtin_bit_cast(float, __builtin_amdgcn_readlane(__builtin_bit_cast(int, rl), i));
;             *(unsigned*)((isk2 ? KF : QF) + (size_t)(t0 + t) * 1024 + h * 128 + 2 * lane) = pk2(x0 * r * (isk2 ? gk0 : gq0), x1 * r * (isk2 ? gk1 : gq1)); }
;     }
;     __syncthreads();
	v_add_f32_e32 v18, v63, v18
	v_fmamk_f32 v18, v18, 0x3c000000, v98
	v_rsq_f32_e32 v18, v18
	v_readlane_b32 s7, v254, 23
	v_readlane_b32 s12, v254, 28
	v_readlane_b32 s13, v254, 29
	v_readlane_b32 s60, v18, 0
	v_readlane_b32 s14, v254, 30
	v_readlane_b32 s15, v254, 31
	v_pk_mul_f32 v[82:83], s[60:61], v[82:83] op_sel_hi:[0,1]
	s_waitcnt vmcnt(2)
	v_pk_mul_f32 v[82:83], v[74:75], v[82:83]
	s_nop 0
	v_cvt_pk_bf16_f32 v63, v82, v83
	global_store_dword v92, v63, s[50:51]
	v_readlane_b32 s50, v18, 1
	s_nop 1
	v_pk_mul_f32 v[78:79], s[50:51], v[78:79] op_sel_hi:[0,1]
	v_readlane_b32 s50, v18, 2
	s_waitcnt vmcnt(2)
	v_pk_mul_f32 v[78:79], v[80:81], v[78:79]
	v_pk_mul_f32 v[76:77], s[50:51], v[76:77] op_sel_hi:[0,1]
	v_readlane_b32 s50, v18, 3
	v_cvt_pk_bf16_f32 v63, v78, v79
	v_pk_mul_f32 v[76:77], v[74:75], v[76:77]
	v_pk_mul_f32 v[72:73], s[50:51], v[72:73] op_sel_hi:[0,1]
	v_readlane_b32 s50, v18, 4
	global_store_dword v92, v63, s[84:85]
	v_cvt_pk_bf16_f32 v63, v76, v77
	v_pk_mul_f32 v[70:71], s[50:51], v[70:71] op_sel_hi:[0,1]
	v_readlane_b32 s50, v18, 5
	v_pk_mul_f32 v[72:73], v[80:81], v[72:73]
	global_store_dword v92, v63, s[80:81]
	v_pk_mul_f32 v[68:69], s[50:51], v[68:69] op_sel_hi:[0,1]
	v_readlane_b32 s50, v18, 6
	v_cvt_pk_bf16_f32 v63, v72, v73
	v_pk_mul_f32 v[70:71], v[74:75], v[70:71]
	v_pk_mul_f32 v[66:67], s[50:51], v[66:67] op_sel_hi:[0,1]
	v_readlane_b32 s50, v18, 7
	global_store_dword v92, v63, s[86:87]
	v_cvt_pk_bf16_f32 v63, v70, v71
	v_pk_mul_f32 v[64:65], s[50:51], v[64:65] op_sel_hi:[0,1]
	v_readlane_b32 s50, v18, 8
	v_pk_mul_f32 v[68:69], v[80:81], v[68:69]
	global_store_dword v92, v63, s[76:77]
	v_pk_mul_f32 v[16:17], s[50:51], v[16:17] op_sel_hi:[0,1]
	v_readlane_b32 s50, v18, 9
	v_cvt_pk_bf16_f32 v63, v68, v69
	v_pk_mul_f32 v[66:67], v[74:75], v[66:67]
	v_pk_mul_f32 v[14:15], s[50:51], v[14:15] op_sel_hi:[0,1]
	v_readlane_b32 s50, v18, 10
	global_store_dword v92, v63, s[92:93]
	v_cvt_pk_bf16_f32 v63, v66, v67
	v_pk_mul_f32 v[12:13], s[50:51], v[12:13] op_sel_hi:[0,1]
	v_readlane_b32 s50, v18, 11
	v_pk_mul_f32 v[64:65], v[80:81], v[64:65]
	v_pk_mul_f32 v[16:17], v[74:75], v[16:17]
	v_pk_mul_f32 v[10:11], s[50:51], v[10:11] op_sel_hi:[0,1]
	v_readlane_b32 s50, v18, 12
	v_pk_mul_f32 v[14:15], v[80:81], v[14:15]
	v_pk_mul_f32 v[12:13], v[74:75], v[12:13]
	v_pk_mul_f32 v[8:9], s[50:51], v[8:9] op_sel_hi:[0,1]
	v_readlane_b32 s50, v18, 13
	v_pk_mul_f32 v[10:11], v[80:81], v[10:11]
	global_store_dword v92, v63, s[72:73]
	v_pk_mul_f32 v[6:7], s[50:51], v[6:7] op_sel_hi:[0,1]
	v_readlane_b32 s50, v18, 14
	v_pk_mul_f32 v[6:7], v[80:81], v[6:7]
	v_cvt_pk_bf16_f32 v63, v64, v65
	v_pk_mul_f32 v[4:5], s[50:51], v[4:5] op_sel_hi:[0,1]
	v_pk_mul_f32 v[4:5], v[74:75], v[4:5]
	v_cvt_pk_bf16_f32 v16, v16, v17
	v_cvt_pk_bf16_f32 v14, v14, v15
	v_cvt_pk_bf16_f32 v12, v12, v13
	v_cvt_pk_bf16_f32 v10, v10, v11
	v_cvt_pk_bf16_f32 v6, v6, v7
	v_cvt_pk_bf16_f32 v4, v4, v5
	global_store_dword v92, v63, s[94:95]
	global_store_dword v92, v16, s[68:69]
	global_store_dword v92, v14, s[96:97]
	global_store_dword v92, v12, s[66:67]
	global_store_dword v92, v10, vcc
	global_store_dword v92, v6, s[90:91]
	global_store_dword v92, v4, s[0:1]
	v_readlane_b32 s0, v18, 15
	v_readlane_b32 s92, v254, 49
	v_pk_mul_f32 v[8:9], v[74:75], v[8:9]
	v_pk_mul_f32 v[2:3], s[0:1], v[2:3] op_sel_hi:[0,1]
	s_add_u32 s0, s53, s48
	s_addc_u32 s1, s54, s49
	s_add_u32 s0, s0, s30
	v_pk_mul_f32 v[2:3], v[80:81], v[2:3]
	s_addc_u32 s1, s1, 0
	s_add_i32 s58, s58, s92
	v_cvt_pk_bf16_f32 v8, v8, v9
	v_cvt_pk_bf16_f32 v2, v2, v3
	s_cmpk_lt_i32 s58, 0x400
	global_store_dword v92, v8, s[64:65]
	global_store_dword v92, v2, s[0:1]
	s_barrier
	s_cbranch_scc0 .LBB0_474

; #define SBAR() __builtin_amdgcn_sched_barrier(0)
; __device__ __forceinline__ int crow(int r, int hi) { return (r & 3) + 8 * (r >> 2) + 4 * hi; }
; #define SEAM_K0() do { VMWN(NQL); if constexpr (F32) { SWRITE_KF(0); SBAR(); SLOAD_F((const float*)nxt.V, kbn); } else { SWRITE_HK(0); } SBAR(); } while (0)
; template <class TIn, class TOut>
; __device__ __forceinline__ void causal_swa_block(const BlockRef<TIn, TOut>& cur, const BlockRef<TIn, TOut>& nxt, int skv, int W, char* lds, Seam<TIn>& S) {
;     ...
;     SBAR(); SEAM_K0();
;     {
;         bf16* Pw = cur.PO + (size_t)(wid * QBLK) * 128;
; #pragma unroll
;         for (int r = 0; r < 16; ++r) { const int orow = crow(r, hi);
; #pragma unroll
;             for (int d0 = 0; d0 < 4; ++d0) { const float v = o[d0][r]; const float vn = __shfl_xor(v, 1);
;                 if ((r32 & 1) == 0) __builtin_nontemporal_store(cvtpk(v, vn), (unsigned*)(Pw + (size_t)orow * 128 + d0 * 32 + r32)); } }
.LBB0_749:
	s_waitcnt vmcnt(8)
	s_waitcnt vmcnt(9)
	ds_write_b128 v224, v[106:109] offset:32768
	s_waitcnt vmcnt(8)
	ds_write_b128 v224, v[110:113] offset:40960
	s_lshl_b64 s[0:1], s[10:11], 8
	v_mov_b32_dpp v68, v50 quad_perm:[1,0,3,2] row_mask:0xf bank_mask:0xf
	s_add_u32 s0, s34, s0
	s_addc_u32 s1, s35, s1
	v_lshlrev_b32_e32 v66, 1, v194
	v_mov_b32_e32 v67, v197
	v_lshl_add_u64 v[66:67], s[0:1], 0, v[66:67]
	v_lshl_add_u64 v[66:67], v[66:67], 0, v[200:201]
	s_and_saveexec_b64 s[0:1], s[4:5]
	s_cbranch_execz .LBB0_751
	s_waitcnt lgkmcnt(0)
	v_cvt_pk_bf16_f32 v50, v50, v68
	global_store_dword v[66:67], v50, off nt
.LBB0_751:
	s_or_b64 exec, exec, s[0:1]
	v_mov_b32_dpp v50, v34 quad_perm:[1,0,3,2] row_mask:0xf bank_mask:0xf
	s_and_saveexec_b64 s[0:1], s[4:5]
	s_cbranch_execz .LBB0_753
	s_waitcnt lgkmcnt(0)
	v_cvt_pk_bf16_f32 v34, v34, v50
	global_store_dword v[66:67], v34, off offset:64 nt
.LBB0_753:
	s_or_b64 exec, exec, s[0:1]
	v_mov_b32_dpp v34, v18 quad_perm:[1,0,3,2] row_mask:0xf bank_mask:0xf
	s_and_saveexec_b64 s[0:1], s[4:5]
	s_cbranch_execz .LBB0_755
	s_waitcnt lgkmcnt(0)
	v_cvt_pk_bf16_f32 v18, v18, v34
	global_store_dword v[66:67], v18, off offset:128 nt
.LBB0_755:
	s_or_b64 exec, exec, s[0:1]
	v_mov_b32_dpp v18, v2 quad_perm:[1,0,3,2] row_mask:0xf bank_mask:0xf
	s_and_saveexec_b64 s[0:1], s[4:5]
	s_cbranch_execz .LBB0_757
	s_waitcnt lgkmcnt(0)
	v_cvt_pk_bf16_f32 v2, v2, v18
	global_store_dword v[66:67], v2, off offset:192 nt
.LBB0_757:
	s_or_b64 exec, exec, s[0:1]
	v_mov_b32_dpp v2, v51 quad_perm:[1,0,3,2] row_mask:0xf bank_mask:0xf
	s_and_saveexec_b64 s[0:1], s[4:5]
	s_cbranch_execz .LBB0_759
	s_waitcnt lgkmcnt(0)
	v_cvt_pk_bf16_f32 v2, v51, v2
	global_store_dword v[66:67], v2, off offset:256 nt
.LBB0_759:
	s_or_b64 exec, exec, s[0:1]
	s_waitcnt lgkmcnt(0)
	v_mov_b32_dpp v2, v35 quad_perm:[1,0,3,2] row_mask:0xf bank_mask:0xf
	s_and_saveexec_b64 s[0:1], s[4:5]
	s_cbranch_execz .LBB0_761
	s_waitcnt lgkmcnt(0)
	v_cvt_pk_bf16_f32 v2, v35, v2
	global_store_dword v[66:67], v2, off offset:320 nt
.LBB0_761:
	s_or_b64 exec, exec, s[0:1]
	s_waitcnt lgkmcnt(0)
	v_mov_b32_dpp v2, v19 quad_perm:[1,0,3,2] row_mask:0xf bank_mask:0xf
	s_and_saveexec_b64 s[0:1], s[4:5]
	s_cbranch_execz .LBB0_763
	s_waitcnt lgkmcnt(0)
	v_cvt_pk_bf16_f32 v2, v19, v2
	global_store_dword v[66:67], v2, off offset:384 nt
.LBB0_763:
	s_or_b64 exec, exec, s[0:1]
	s_waitcnt lgkmcnt(0)
	v_mov_b32_dpp v2, v3 quad_perm:[1,0,3,2] row_mask:0xf bank_mask:0xf
	s_and_saveexec_b64 s[0:1], s[4:5]
	s_cbranch_execz .LBB0_765
	s_waitcnt lgkmcnt(0)
	v_cvt_pk_bf16_f32 v2, v3, v2
	global_store_dword v[66:67], v2, off offset:448 nt
.LBB0_765:
	s_or_b64 exec, exec, s[0:1]
	s_waitcnt lgkmcnt(0)
	v_mov_b32_dpp v2, v52 quad_perm:[1,0,3,2] row_mask:0xf bank_mask:0xf
	s_and_saveexec_b64 s[0:1], s[4:5]
	s_cbranch_execz .LBB0_767
	s_waitcnt lgkmcnt(0)
	v_cvt_pk_bf16_f32 v2, v52, v2
	global_store_dword v[66:67], v2, off offset:512 nt
.LBB0_767:
	s_or_b64 exec, exec, s[0:1]
	s_waitcnt lgkmcnt(0)
	v_mov_b32_dpp v2, v36 quad_perm:[1,0,3,2] row_mask:0xf bank_mask:0xf
	s_and_saveexec_b64 s[0:1], s[4:5]
	s_cbranch_execz .LBB0_769
	s_waitcnt lgkmcnt(0)
	v_cvt_pk_bf16_f32 v2, v36, v2
	global_store_dword v[66:67], v2, off offset:576 nt
.LBB0_769:
	s_or_b64 exec, exec, s[0:1]
	s_waitcnt lgkmcnt(0)
	v_mov_b32_dpp v2, v20 quad_perm:[1,0,3,2] row_mask:0xf bank_mask:0xf
	s_and_saveexec_b64 s[0:1], s[4:5]
	s_cbranch_execz .LBB0_771
	s_waitcnt lgkmcnt(0)
	v_cvt_pk_bf16_f32 v2, v20, v2
	global_store_dword v[66:67], v2, off offset:640 nt
.LBB0_771:
	s_or_b64 exec, exec, s[0:1]
	s_waitcnt lgkmcnt(0)
	v_mov_b32_dpp v2, v4 quad_perm:[1,0,3,2] row_mask:0xf bank_mask:0xf
	s_and_saveexec_b64 s[0:1], s[4:5]
	s_cbranch_execz .LBB0_773
	s_waitcnt lgkmcnt(0)
	v_cvt_pk_bf16_f32 v2, v4, v2
	global_store_dword v[66:67], v2, off offset:704 nt
.LBB0_773:
	s_or_b64 exec, exec, s[0:1]
	s_waitcnt lgkmcnt(0)
	v_mov_b32_dpp v2, v53 quad_perm:[1,0,3,2] row_mask:0xf bank_mask:0xf
	s_and_saveexec_b64 s[0:1], s[4:5]
	s_cbranch_execz .LBB0_775
	s_waitcnt lgkmcnt(0)
	v_cvt_pk_bf16_f32 v2, v53, v2
	global_store_dword v[66:67], v2, off offset:768 nt
.LBB0_775:
	s_or_b64 exec, exec, s[0:1]
	s_waitcnt lgkmcnt(0)
	v_mov_b32_dpp v2, v37 quad_perm:[1,0,3,2] row_mask:0xf bank_mask:0xf
	s_and_saveexec_b64 s[0:1], s[4:5]
	s_cbranch_execz .LBB0_777
	s_waitcnt lgkmcnt(0)
	v_cvt_pk_bf16_f32 v2, v37, v2
	global_store_dword v[66:67], v2, off offset:832 nt
.LBB0_777:
	s_or_b64 exec, exec, s[0:1]
	s_waitcnt lgkmcnt(0)
	v_mov_b32_dpp v2, v21 quad_perm:[1,0,3,2] row_mask:0xf bank_mask:0xf
	s_and_saveexec_b64 s[0:1], s[4:5]
	s_cbranch_execz .LBB0_779
	s_waitcnt lgkmcnt(0)
	v_cvt_pk_bf16_f32 v2, v21, v2
	global_store_dword v[66:67], v2, off offset:896 nt
.LBB0_779:
	s_or_b64 exec, exec, s[0:1]
	s_waitcnt lgkmcnt(0)
	v_mov_b32_dpp v2, v5 quad_perm:[1,0,3,2] row_mask:0xf bank_mask:0xf
	s_and_saveexec_b64 s[0:1], s[4:5]
	s_cbranch_execz .LBB0_781
	s_waitcnt lgkmcnt(0)
	v_cvt_pk_bf16_f32 v2, v5, v2
	global_store_dword v[66:67], v2, off offset:960 nt
.LBB0_781:
	s_or_b64 exec, exec, s[0:1]
	s_waitcnt lgkmcnt(0)
	v_mov_b32_dpp v2, v54 quad_perm:[1,0,3,2] row_mask:0xf bank_mask:0xf
	s_and_saveexec_b64 s[0:1], s[4:5]
	s_cbranch_execz .LBB0_783
	s_waitcnt lgkmcnt(0)
	v_cvt_pk_bf16_f32 v2, v54, v2
	global_store_dword v[66:67], v2, off offset:2048 nt
.LBB0_783:
	s_or_b64 exec, exec, s[0:1]
	s_waitcnt lgkmcnt(0)
	v_mov_b32_dpp v2, v38 quad_perm:[1,0,3,2] row_mask:0xf bank_mask:0xf
	s_and_saveexec_b64 s[0:1], s[4:5]
	s_cbranch_execz .LBB0_785
	s_waitcnt lgkmcnt(0)
	v_cvt_pk_bf16_f32 v2, v38, v2
	global_store_dword v[66:67], v2, off offset:2112 nt
; __device__ __forceinline__ int crow(int r, int hi) { return (r & 3) + 8 * (r >> 2) + 4 * hi; }
; template <class TIn, class TOut>
; __device__ __forceinline__ void causal_swa_block(const BlockRef<TIn, TOut>& cur, const BlockRef<TIn, TOut>& nxt, int skv, int W, char* lds, Seam<TIn>& S) {
;     ...
;         bf16* Pw = cur.PO + (size_t)(wid * QBLK) * 128;
; #pragma unroll
;         for (int r = 0; r < 16; ++r) { const int orow = crow(r, hi);
; #pragma unroll
;             for (int d0 = 0; d0 < 4; ++d0) { const float v = o[d0][r]; const float vn = __shfl_xor(v, 1);
;                 if ((r32 & 1) == 0) __builtin_nontemporal_store(cvtpk(v, vn), (unsigned*)(Pw + (size_t)orow * 128 + d0 * 32 + r32)); } }
.LBB0_785:
	s_or_b64 exec, exec, s[0:1]
	s_waitcnt lgkmcnt(0)
	v_mov_b32_dpp v2, v22 quad_perm:[1,0,3,2] row_mask:0xf bank_mask:0xf
	s_and_saveexec_b64 s[0:1], s[4:5]
	s_cbranch_execz .LBB0_787
	s_waitcnt lgkmcnt(0)
	v_cvt_pk_bf16_f32 v2, v22, v2
	global_store_dword v[66:67], v2, off offset:2176 nt
.LBB0_787:
	s_or_b64 exec, exec, s[0:1]
	s_waitcnt lgkmcnt(0)
	v_mov_b32_dpp v2, v6 quad_perm:[1,0,3,2] row_mask:0xf bank_mask:0xf
	s_and_saveexec_b64 s[0:1], s[4:5]
	s_cbranch_execz .LBB0_789
	s_waitcnt lgkmcnt(0)
	v_cvt_pk_bf16_f32 v2, v6, v2
	global_store_dword v[66:67], v2, off offset:2240 nt
.LBB0_789:
	s_or_b64 exec, exec, s[0:1]
	s_waitcnt lgkmcnt(0)
	v_mov_b32_dpp v2, v55 quad_perm:[1,0,3,2] row_mask:0xf bank_mask:0xf
	s_and_saveexec_b64 s[0:1], s[4:5]
	s_cbranch_execz .LBB0_791
	s_waitcnt lgkmcnt(0)
	v_cvt_pk_bf16_f32 v2, v55, v2
	global_store_dword v[66:67], v2, off offset:2304 nt
.LBB0_791:
	s_or_b64 exec, exec, s[0:1]
	s_waitcnt lgkmcnt(0)
	v_mov_b32_dpp v2, v39 quad_perm:[1,0,3,2] row_mask:0xf bank_mask:0xf
	s_and_saveexec_b64 s[0:1], s[4:5]
	s_cbranch_execz .LBB0_793
	s_waitcnt lgkmcnt(0)
	v_cvt_pk_bf16_f32 v2, v39, v2
	global_store_dword v[66:67], v2, off offset:2368 nt
.LBB0_793:
	s_or_b64 exec, exec, s[0:1]
	s_waitcnt lgkmcnt(0)
	v_mov_b32_dpp v2, v23 quad_perm:[1,0,3,2] row_mask:0xf bank_mask:0xf
	s_and_saveexec_b64 s[0:1], s[4:5]
	s_cbranch_execz .LBB0_795
	s_waitcnt lgkmcnt(0)
	v_cvt_pk_bf16_f32 v2, v23, v2
	global_store_dword v[66:67], v2, off offset:2432 nt
.LBB0_795:
	s_or_b64 exec, exec, s[0:1]
	s_waitcnt lgkmcnt(0)
	v_mov_b32_dpp v2, v7 quad_perm:[1,0,3,2] row_mask:0xf bank_mask:0xf
	s_and_saveexec_b64 s[0:1], s[4:5]
	s_cbranch_execz .LBB0_797
	s_waitcnt lgkmcnt(0)
	v_cvt_pk_bf16_f32 v2, v7, v2
	global_store_dword v[66:67], v2, off offset:2496 nt
.LBB0_797:
	s_or_b64 exec, exec, s[0:1]
	s_waitcnt lgkmcnt(0)
	v_mov_b32_dpp v2, v56 quad_perm:[1,0,3,2] row_mask:0xf bank_mask:0xf
	s_and_saveexec_b64 s[0:1], s[4:5]
	s_cbranch_execz .LBB0_799
	s_waitcnt lgkmcnt(0)
	v_cvt_pk_bf16_f32 v2, v56, v2
	global_store_dword v[66:67], v2, off offset:2560 nt
.LBB0_799:
	s_or_b64 exec, exec, s[0:1]
	s_waitcnt lgkmcnt(0)
	v_mov_b32_dpp v2, v40 quad_perm:[1,0,3,2] row_mask:0xf bank_mask:0xf
	s_and_saveexec_b64 s[0:1], s[4:5]
	s_cbranch_execz .LBB0_801
	s_waitcnt lgkmcnt(0)
	v_cvt_pk_bf16_f32 v2, v40, v2
	global_store_dword v[66:67], v2, off offset:2624 nt
.LBB0_801:
	s_or_b64 exec, exec, s[0:1]
	s_waitcnt lgkmcnt(0)
	v_mov_b32_dpp v2, v24 quad_perm:[1,0,3,2] row_mask:0xf bank_mask:0xf
	s_and_saveexec_b64 s[0:1], s[4:5]
	s_cbranch_execz .LBB0_803
	s_waitcnt lgkmcnt(0)
	v_cvt_pk_bf16_f32 v2, v24, v2
	global_store_dword v[66:67], v2, off offset:2688 nt
.LBB0_803:
	s_or_b64 exec, exec, s[0:1]
	s_waitcnt lgkmcnt(0)
	v_mov_b32_dpp v2, v8 quad_perm:[1,0,3,2] row_mask:0xf bank_mask:0xf
	s_and_saveexec_b64 s[0:1], s[4:5]
	s_cbranch_execz .LBB0_805
	s_waitcnt lgkmcnt(0)
	v_cvt_pk_bf16_f32 v2, v8, v2
	global_store_dword v[66:67], v2, off offset:2752 nt
.LBB0_805:
	s_or_b64 exec, exec, s[0:1]
	s_waitcnt lgkmcnt(0)
	v_mov_b32_dpp v2, v57 quad_perm:[1,0,3,2] row_mask:0xf bank_mask:0xf
	s_and_saveexec_b64 s[0:1], s[4:5]
	s_cbranch_execz .LBB0_807
	s_waitcnt lgkmcnt(0)
	v_cvt_pk_bf16_f32 v2, v57, v2
	global_store_dword v[66:67], v2, off offset:2816 nt
.LBB0_807:
	s_or_b64 exec, exec, s[0:1]
	s_waitcnt lgkmcnt(0)
	v_mov_b32_dpp v2, v41 quad_perm:[1,0,3,2] row_mask:0xf bank_mask:0xf
	s_and_saveexec_b64 s[0:1], s[4:5]
	s_cbranch_execz .LBB0_809
	s_waitcnt lgkmcnt(0)
	v_cvt_pk_bf16_f32 v2, v41, v2
	global_store_dword v[66:67], v2, off offset:2880 nt
.LBB0_809:
	s_or_b64 exec, exec, s[0:1]
	s_waitcnt lgkmcnt(0)
	v_mov_b32_dpp v2, v25 quad_perm:[1,0,3,2] row_mask:0xf bank_mask:0xf
	s_and_saveexec_b64 s[0:1], s[4:5]
	s_cbranch_execz .LBB0_811
	s_waitcnt lgkmcnt(0)
	v_cvt_pk_bf16_f32 v2, v25, v2
	global_store_dword v[66:67], v2, off offset:2944 nt
.LBB0_811:
	s_or_b64 exec, exec, s[0:1]
	s_waitcnt lgkmcnt(0)
	v_mov_b32_dpp v2, v9 quad_perm:[1,0,3,2] row_mask:0xf bank_mask:0xf
	s_and_saveexec_b64 s[0:1], s[4:5]
	s_cbranch_execz .LBB0_813
	s_waitcnt lgkmcnt(0)
	v_cvt_pk_bf16_f32 v2, v9, v2
	global_store_dword v[66:67], v2, off offset:3008 nt
.LBB0_813:
	s_or_b64 exec, exec, s[0:1]
	s_waitcnt lgkmcnt(0)
	v_mov_b32_dpp v2, v58 quad_perm:[1,0,3,2] row_mask:0xf bank_mask:0xf
	s_and_saveexec_b64 s[0:1], s[4:5]
	s_cbranch_execz .LBB0_815
	s_waitcnt lgkmcnt(0)
	v_cvt_pk_bf16_f32 v4, v58, v2
	v_add_co_u32_e32 v2, vcc, 0x1000, v66
	s_nop 1
	v_addc_co_u32_e32 v3, vcc, 0, v67, vcc
	global_store_dword v[2:3], v4, off nt
.LBB0_815:
	s_or_b64 exec, exec, s[0:1]
	s_waitcnt lgkmcnt(0)
	v_mov_b32_dpp v2, v42 quad_perm:[1,0,3,2] row_mask:0xf bank_mask:0xf
	s_and_saveexec_b64 s[0:1], s[4:5]
	s_cbranch_execz .LBB0_817
	s_waitcnt lgkmcnt(0)
	v_cvt_pk_bf16_f32 v4, v42, v2
	v_add_co_u32_e32 v2, vcc, 0x1000, v66
	s_nop 1
	v_addc_co_u32_e32 v3, vcc, 0, v67, vcc
	global_store_dword v[2:3], v4, off offset:64 nt
.LBB0_817:
	s_or_b64 exec, exec, s[0:1]
	s_waitcnt lgkmcnt(0)
	v_mov_b32_dpp v2, v26 quad_perm:[1,0,3,2] row_mask:0xf bank_mask:0xf
	s_and_saveexec_b64 s[0:1], s[4:5]
	s_cbranch_execz .LBB0_819
	s_waitcnt lgkmcnt(0)
	v_cvt_pk_bf16_f32 v4, v26, v2
	v_add_co_u32_e32 v2, vcc, 0x1000, v66
	s_nop 1
	v_addc_co_u32_e32 v3, vcc, 0, v67, vcc
	global_store_dword v[2:3], v4, off offset:128 nt
.LBB0_819:
	s_or_b64 exec, exec, s[0:1]
	s_waitcnt lgkmcnt(0)
	v_mov_b32_dpp v2, v10 quad_perm:[1,0,3,2] row_mask:0xf bank_mask:0xf
	s_and_saveexec_b64 s[0:1], s[4:5]
	s_cbranch_execz .LBB0_821
	s_waitcnt lgkmcnt(0)
	v_cvt_pk_bf16_f32 v4, v10, v2
	v_add_co_u32_e32 v2, vcc, 0x1000, v66
	s_nop 1
	v_addc_co_u32_e32 v3, vcc, 0, v67, vcc
	global_store_dword v[2:3], v4, off offset:192 nt
; __device__ __forceinline__ int crow(int r, int hi) { return (r & 3) + 8 * (r >> 2) + 4 * hi; }
; template <class TIn, class TOut>
; __device__ __forceinline__ void causal_swa_block(const BlockRef<TIn, TOut>& cur, const BlockRef<TIn, TOut>& nxt, int skv, int W, char* lds, Seam<TIn>& S) {
;     ...
;         bf16* Pw = cur.PO + (size_t)(wid * QBLK) * 128;
; #pragma unroll
;         for (int r = 0; r < 16; ++r) { const int orow = crow(r, hi);
; #pragma unroll
;             for (int d0 = 0; d0 < 4; ++d0) { const float v = o[d0][r]; const float vn = __shfl_xor(v, 1);
;                 if ((r32 & 1) == 0) __builtin_nontemporal_store(cvtpk(v, vn), (unsigned*)(Pw + (size_t)orow * 128 + d0 * 32 + r32)); } }
.LBB0_821:
	s_or_b64 exec, exec, s[0:1]
	s_waitcnt lgkmcnt(0)
	v_mov_b32_dpp v2, v59 quad_perm:[1,0,3,2] row_mask:0xf bank_mask:0xf
	s_and_saveexec_b64 s[0:1], s[4:5]
	s_cbranch_execz .LBB0_823
	s_waitcnt lgkmcnt(0)
	v_cvt_pk_bf16_f32 v4, v59, v2
	v_add_co_u32_e32 v2, vcc, 0x1000, v66
	s_nop 1
	v_addc_co_u32_e32 v3, vcc, 0, v67, vcc
	global_store_dword v[2:3], v4, off offset:256 nt
.LBB0_823:
	s_or_b64 exec, exec, s[0:1]
	s_waitcnt lgkmcnt(0)
	v_mov_b32_dpp v2, v43 quad_perm:[1,0,3,2] row_mask:0xf bank_mask:0xf
	s_and_saveexec_b64 s[0:1], s[4:5]
	s_cbranch_execz .LBB0_825
	s_waitcnt lgkmcnt(0)
	v_cvt_pk_bf16_f32 v4, v43, v2
	v_add_co_u32_e32 v2, vcc, 0x1000, v66
	s_nop 1
	v_addc_co_u32_e32 v3, vcc, 0, v67, vcc
	global_store_dword v[2:3], v4, off offset:320 nt
.LBB0_825:
	s_or_b64 exec, exec, s[0:1]
	s_waitcnt lgkmcnt(0)
	v_mov_b32_dpp v2, v27 quad_perm:[1,0,3,2] row_mask:0xf bank_mask:0xf
	s_and_saveexec_b64 s[0:1], s[4:5]
	s_cbranch_execz .LBB0_827
	s_waitcnt lgkmcnt(0)
	v_cvt_pk_bf16_f32 v4, v27, v2
	v_add_co_u32_e32 v2, vcc, 0x1000, v66
	s_nop 1
	v_addc_co_u32_e32 v3, vcc, 0, v67, vcc
	global_store_dword v[2:3], v4, off offset:384 nt
.LBB0_827:
	s_or_b64 exec, exec, s[0:1]
	s_waitcnt lgkmcnt(0)
	v_mov_b32_dpp v2, v11 quad_perm:[1,0,3,2] row_mask:0xf bank_mask:0xf
	s_and_saveexec_b64 s[0:1], s[4:5]
	s_cbranch_execz .LBB0_829
	s_waitcnt lgkmcnt(0)
	v_cvt_pk_bf16_f32 v4, v11, v2
	v_add_co_u32_e32 v2, vcc, 0x1000, v66
	s_nop 1
	v_addc_co_u32_e32 v3, vcc, 0, v67, vcc
	global_store_dword v[2:3], v4, off offset:448 nt
.LBB0_829:
	s_or_b64 exec, exec, s[0:1]
	s_waitcnt lgkmcnt(0)
	v_mov_b32_dpp v2, v60 quad_perm:[1,0,3,2] row_mask:0xf bank_mask:0xf
	s_and_saveexec_b64 s[0:1], s[4:5]
	s_cbranch_execz .LBB0_831
	s_waitcnt lgkmcnt(0)
	v_cvt_pk_bf16_f32 v4, v60, v2
	v_add_co_u32_e32 v2, vcc, 0x1000, v66
	s_nop 1
	v_addc_co_u32_e32 v3, vcc, 0, v67, vcc
	global_store_dword v[2:3], v4, off offset:512 nt
.LBB0_831:
	s_or_b64 exec, exec, s[0:1]
	s_waitcnt lgkmcnt(0)
	v_mov_b32_dpp v2, v44 quad_perm:[1,0,3,2] row_mask:0xf bank_mask:0xf
	s_and_saveexec_b64 s[0:1], s[4:5]
	s_cbranch_execz .LBB0_833
	s_waitcnt lgkmcnt(0)
	v_cvt_pk_bf16_f32 v4, v44, v2
	v_add_co_u32_e32 v2, vcc, 0x1000, v66
	s_nop 1
	v_addc_co_u32_e32 v3, vcc, 0, v67, vcc
	global_store_dword v[2:3], v4, off offset:576 nt
.LBB0_833:
	s_or_b64 exec, exec, s[0:1]
	s_waitcnt lgkmcnt(0)
	v_mov_b32_dpp v2, v28 quad_perm:[1,0,3,2] row_mask:0xf bank_mask:0xf
	s_and_saveexec_b64 s[0:1], s[4:5]
	s_cbranch_execz .LBB0_835
	s_waitcnt lgkmcnt(0)
	v_cvt_pk_bf16_f32 v4, v28, v2
	v_add_co_u32_e32 v2, vcc, 0x1000, v66
	s_nop 1
	v_addc_co_u32_e32 v3, vcc, 0, v67, vcc
	global_store_dword v[2:3], v4, off offset:640 nt
.LBB0_835:
	s_or_b64 exec, exec, s[0:1]
	s_waitcnt lgkmcnt(0)
	v_mov_b32_dpp v2, v12 quad_perm:[1,0,3,2] row_mask:0xf bank_mask:0xf
	s_and_saveexec_b64 s[0:1], s[4:5]
	s_cbranch_execz .LBB0_837
	s_waitcnt lgkmcnt(0)
	v_cvt_pk_bf16_f32 v4, v12, v2
	v_add_co_u32_e32 v2, vcc, 0x1000, v66
	s_nop 1
	v_addc_co_u32_e32 v3, vcc, 0, v67, vcc
	global_store_dword v[2:3], v4, off offset:704 nt
.LBB0_837:
	s_or_b64 exec, exec, s[0:1]
	s_waitcnt lgkmcnt(0)
	v_mov_b32_dpp v2, v61 quad_perm:[1,0,3,2] row_mask:0xf bank_mask:0xf
	s_and_saveexec_b64 s[0:1], s[4:5]
	s_cbranch_execz .LBB0_839
	s_waitcnt lgkmcnt(0)
	v_cvt_pk_bf16_f32 v4, v61, v2
	v_add_co_u32_e32 v2, vcc, 0x1000, v66
	s_nop 1
	v_addc_co_u32_e32 v3, vcc, 0, v67, vcc
	global_store_dword v[2:3], v4, off offset:768 nt
.LBB0_839:
	s_or_b64 exec, exec, s[0:1]
	s_waitcnt lgkmcnt(0)
	v_mov_b32_dpp v2, v45 quad_perm:[1,0,3,2] row_mask:0xf bank_mask:0xf
	s_and_saveexec_b64 s[0:1], s[4:5]
	s_cbranch_execz .LBB0_841
	s_waitcnt lgkmcnt(0)
	v_cvt_pk_bf16_f32 v4, v45, v2
	v_add_co_u32_e32 v2, vcc, 0x1000, v66
	s_nop 1
	v_addc_co_u32_e32 v3, vcc, 0, v67, vcc
	global_store_dword v[2:3], v4, off offset:832 nt
.LBB0_841:
	s_or_b64 exec, exec, s[0:1]
	s_waitcnt lgkmcnt(0)
	v_mov_b32_dpp v2, v29 quad_perm:[1,0,3,2] row_mask:0xf bank_mask:0xf
	s_and_saveexec_b64 s[0:1], s[4:5]
	s_cbranch_execz .LBB0_843
	s_waitcnt lgkmcnt(0)
	v_cvt_pk_bf16_f32 v4, v29, v2
	v_add_co_u32_e32 v2, vcc, 0x1000, v66
	s_nop 1
	v_addc_co_u32_e32 v3, vcc, 0, v67, vcc
	global_store_dword v[2:3], v4, off offset:896 nt
.LBB0_843:
	s_or_b64 exec, exec, s[0:1]
	s_waitcnt lgkmcnt(0)
	v_mov_b32_dpp v2, v13 quad_perm:[1,0,3,2] row_mask:0xf bank_mask:0xf
	s_and_saveexec_b64 s[0:1], s[4:5]
	s_cbranch_execz .LBB0_845
	s_waitcnt lgkmcnt(0)
	v_cvt_pk_bf16_f32 v4, v13, v2
	v_add_co_u32_e32 v2, vcc, 0x1000, v66
	s_nop 1
	v_addc_co_u32_e32 v3, vcc, 0, v67, vcc
	global_store_dword v[2:3], v4, off offset:960 nt
.LBB0_845:
	s_or_b64 exec, exec, s[0:1]
	s_waitcnt lgkmcnt(0)
	v_mov_b32_dpp v2, v62 quad_perm:[1,0,3,2] row_mask:0xf bank_mask:0xf
	s_and_saveexec_b64 s[0:1], s[4:5]
	s_cbranch_execz .LBB0_847
	s_waitcnt lgkmcnt(0)
	v_cvt_pk_bf16_f32 v4, v62, v2
	v_add_co_u32_e32 v2, vcc, 0x1000, v66
	s_nop 1
	v_addc_co_u32_e32 v3, vcc, 0, v67, vcc
	global_store_dword v[2:3], v4, off offset:2048 nt
.LBB0_847:
	s_or_b64 exec, exec, s[0:1]
	s_waitcnt lgkmcnt(0)
	v_mov_b32_dpp v2, v46 quad_perm:[1,0,3,2] row_mask:0xf bank_mask:0xf
	s_and_saveexec_b64 s[0:1], s[4:5]
	s_cbranch_execz .LBB0_849
	s_waitcnt lgkmcnt(0)
	v_cvt_pk_bf16_f32 v4, v46, v2
	v_add_co_u32_e32 v2, vcc, 0x1000, v66
	s_nop 1
	v_addc_co_u32_e32 v3, vcc, 0, v67, vcc
	global_store_dword v[2:3], v4, off offset:2112 nt
; __device__ __forceinline__ int crow(int r, int hi) { return (r & 3) + 8 * (r >> 2) + 4 * hi; }
; template <class TIn, class TOut>
; __device__ __forceinline__ void causal_swa_block(const BlockRef<TIn, TOut>& cur, const BlockRef<TIn, TOut>& nxt, int skv, int W, char* lds, Seam<TIn>& S) {
;     ...
;         bf16* Pw = cur.PO + (size_t)(wid * QBLK) * 128;
; #pragma unroll
;         for (int r = 0; r < 16; ++r) { const int orow = crow(r, hi);
; #pragma unroll
;             for (int d0 = 0; d0 < 4; ++d0) { const float v = o[d0][r]; const float vn = __shfl_xor(v, 1);
;                 if ((r32 & 1) == 0) __builtin_nontemporal_store(cvtpk(v, vn), (unsigned*)(Pw + (size_t)orow * 128 + d0 * 32 + r32)); } }
.LBB0_849:
	s_or_b64 exec, exec, s[0:1]
	s_waitcnt lgkmcnt(0)
	v_mov_b32_dpp v2, v30 quad_perm:[1,0,3,2] row_mask:0xf bank_mask:0xf
	s_and_saveexec_b64 s[0:1], s[4:5]
	s_cbranch_execz .LBB0_851
	s_waitcnt lgkmcnt(0)
	v_cvt_pk_bf16_f32 v4, v30, v2
	v_add_co_u32_e32 v2, vcc, 0x1000, v66
	s_nop 1
	v_addc_co_u32_e32 v3, vcc, 0, v67, vcc
	global_store_dword v[2:3], v4, off offset:2176 nt
.LBB0_851:
	s_or_b64 exec, exec, s[0:1]
	s_waitcnt lgkmcnt(0)
	v_mov_b32_dpp v2, v14 quad_perm:[1,0,3,2] row_mask:0xf bank_mask:0xf
	s_and_saveexec_b64 s[0:1], s[4:5]
	s_cbranch_execz .LBB0_853
	s_waitcnt lgkmcnt(0)
	v_cvt_pk_bf16_f32 v4, v14, v2
	v_add_co_u32_e32 v2, vcc, 0x1000, v66
	s_nop 1
	v_addc_co_u32_e32 v3, vcc, 0, v67, vcc
	global_store_dword v[2:3], v4, off offset:2240 nt
.LBB0_853:
	s_or_b64 exec, exec, s[0:1]
	s_waitcnt lgkmcnt(0)
	v_mov_b32_dpp v2, v63 quad_perm:[1,0,3,2] row_mask:0xf bank_mask:0xf
	s_and_saveexec_b64 s[0:1], s[4:5]
	s_cbranch_execz .LBB0_855
	s_waitcnt lgkmcnt(0)
	v_cvt_pk_bf16_f32 v4, v63, v2
	v_add_co_u32_e32 v2, vcc, 0x1000, v66
	s_nop 1
	v_addc_co_u32_e32 v3, vcc, 0, v67, vcc
	global_store_dword v[2:3], v4, off offset:2304 nt
.LBB0_855:
	s_or_b64 exec, exec, s[0:1]
	s_waitcnt lgkmcnt(0)
	v_mov_b32_dpp v2, v47 quad_perm:[1,0,3,2] row_mask:0xf bank_mask:0xf
	s_and_saveexec_b64 s[0:1], s[4:5]
	s_cbranch_execz .LBB0_857
	s_waitcnt lgkmcnt(0)
	v_cvt_pk_bf16_f32 v4, v47, v2
	v_add_co_u32_e32 v2, vcc, 0x1000, v66
	s_nop 1
	v_addc_co_u32_e32 v3, vcc, 0, v67, vcc
	global_store_dword v[2:3], v4, off offset:2368 nt
.LBB0_857:
	s_or_b64 exec, exec, s[0:1]
	s_waitcnt lgkmcnt(0)
	v_mov_b32_dpp v2, v31 quad_perm:[1,0,3,2] row_mask:0xf bank_mask:0xf
	s_and_saveexec_b64 s[0:1], s[4:5]
	s_cbranch_execz .LBB0_859
	s_waitcnt lgkmcnt(0)
	v_cvt_pk_bf16_f32 v4, v31, v2
	v_add_co_u32_e32 v2, vcc, 0x1000, v66
	s_nop 1
	v_addc_co_u32_e32 v3, vcc, 0, v67, vcc
	global_store_dword v[2:3], v4, off offset:2432 nt
.LBB0_859:
	s_or_b64 exec, exec, s[0:1]
	s_waitcnt lgkmcnt(0)
	v_mov_b32_dpp v2, v15 quad_perm:[1,0,3,2] row_mask:0xf bank_mask:0xf
	s_and_saveexec_b64 s[0:1], s[4:5]
	s_cbranch_execz .LBB0_861
	s_waitcnt lgkmcnt(0)
	v_cvt_pk_bf16_f32 v4, v15, v2
	v_add_co_u32_e32 v2, vcc, 0x1000, v66
	s_nop 1
	v_addc_co_u32_e32 v3, vcc, 0, v67, vcc
	global_store_dword v[2:3], v4, off offset:2496 nt
.LBB0_861:
	s_or_b64 exec, exec, s[0:1]
	s_waitcnt lgkmcnt(0)
	v_mov_b32_dpp v2, v64 quad_perm:[1,0,3,2] row_mask:0xf bank_mask:0xf
	s_and_saveexec_b64 s[0:1], s[4:5]
	s_cbranch_execz .LBB0_863
	s_waitcnt lgkmcnt(0)
	v_cvt_pk_bf16_f32 v4, v64, v2
	v_add_co_u32_e32 v2, vcc, 0x1000, v66
	s_nop 1
	v_addc_co_u32_e32 v3, vcc, 0, v67, vcc
	global_store_dword v[2:3], v4, off offset:2560 nt
.LBB0_863:
	s_or_b64 exec, exec, s[0:1]
	s_waitcnt lgkmcnt(0)
	v_mov_b32_dpp v2, v48 quad_perm:[1,0,3,2] row_mask:0xf bank_mask:0xf
	s_and_saveexec_b64 s[0:1], s[4:5]
	s_cbranch_execz .LBB0_865
	s_waitcnt lgkmcnt(0)
	v_cvt_pk_bf16_f32 v4, v48, v2
	v_add_co_u32_e32 v2, vcc, 0x1000, v66
	s_nop 1
	v_addc_co_u32_e32 v3, vcc, 0, v67, vcc
	global_store_dword v[2:3], v4, off offset:2624 nt
.LBB0_865:
	s_or_b64 exec, exec, s[0:1]
	s_waitcnt lgkmcnt(0)
	v_mov_b32_dpp v2, v32 quad_perm:[1,0,3,2] row_mask:0xf bank_mask:0xf
	s_and_saveexec_b64 s[0:1], s[4:5]
	s_cbranch_execz .LBB0_867
	s_waitcnt lgkmcnt(0)
	v_cvt_pk_bf16_f32 v4, v32, v2
	v_add_co_u32_e32 v2, vcc, 0x1000, v66
	s_nop 1
	v_addc_co_u32_e32 v3, vcc, 0, v67, vcc
	global_store_dword v[2:3], v4, off offset:2688 nt
.LBB0_867:
	s_or_b64 exec, exec, s[0:1]
	s_waitcnt lgkmcnt(0)
	v_mov_b32_dpp v2, v16 quad_perm:[1,0,3,2] row_mask:0xf bank_mask:0xf
	s_and_saveexec_b64 s[0:1], s[4:5]
	s_cbranch_execz .LBB0_869
	s_waitcnt lgkmcnt(0)
	v_cvt_pk_bf16_f32 v4, v16, v2
	v_add_co_u32_e32 v2, vcc, 0x1000, v66
	s_nop 1
	v_addc_co_u32_e32 v3, vcc, 0, v67, vcc
	global_store_dword v[2:3], v4, off offset:2752 nt
.LBB0_869:
	s_or_b64 exec, exec, s[0:1]
	s_waitcnt lgkmcnt(0)
	v_mov_b32_dpp v2, v65 quad_perm:[1,0,3,2] row_mask:0xf bank_mask:0xf
	s_and_saveexec_b64 s[0:1], s[4:5]
	s_cbranch_execz .LBB0_871
	s_waitcnt lgkmcnt(0)
	v_cvt_pk_bf16_f32 v4, v65, v2
	v_add_co_u32_e32 v2, vcc, 0x1000, v66
	s_nop 1
	v_addc_co_u32_e32 v3, vcc, 0, v67, vcc
	global_store_dword v[2:3], v4, off offset:2816 nt
.LBB0_871:
	s_or_b64 exec, exec, s[0:1]
	s_waitcnt lgkmcnt(0)
	v_mov_b32_dpp v2, v49 quad_perm:[1,0,3,2] row_mask:0xf bank_mask:0xf
	s_and_saveexec_b64 s[0:1], s[4:5]
	s_cbranch_execz .LBB0_873
	s_waitcnt lgkmcnt(0)
	v_cvt_pk_bf16_f32 v4, v49, v2
	v_add_co_u32_e32 v2, vcc, 0x1000, v66
	s_nop 1
	v_addc_co_u32_e32 v3, vcc, 0, v67, vcc
	global_store_dword v[2:3], v4, off offset:2880 nt
.LBB0_873:
	s_or_b64 exec, exec, s[0:1]
	s_waitcnt lgkmcnt(0)
	v_mov_b32_dpp v2, v33 quad_perm:[1,0,3,2] row_mask:0xf bank_mask:0xf
	s_and_saveexec_b64 s[0:1], s[4:5]
	s_cbranch_execz .LBB0_875
	s_waitcnt lgkmcnt(0)
	v_cvt_pk_bf16_f32 v4, v33, v2
	v_add_co_u32_e32 v2, vcc, 0x1000, v66
	s_nop 1
	v_addc_co_u32_e32 v3, vcc, 0, v67, vcc
	global_store_dword v[2:3], v4, off offset:2944 nt
.LBB0_875:
	s_or_b64 exec, exec, s[0:1]
	s_waitcnt lgkmcnt(0)
	v_mov_b32_dpp v2, v17 quad_perm:[1,0,3,2] row_mask:0xf bank_mask:0xf
	s_and_saveexec_b64 s[0:1], s[4:5]
	s_cbranch_execz .LBB0_877
	s_waitcnt lgkmcnt(0)
	v_cvt_pk_bf16_f32 v4, v17, v2
	v_add_co_u32_e32 v2, vcc, 0x1000, v66
	s_nop 1
	v_addc_co_u32_e32 v3, vcc, 0, v67, vcc
	global_store_dword v[2:3], v4, off offset:3008 nt
